# speedup vs baseline: 1.0207x; 1.0097x over previous
.LBB1_19:
	ds_read_b128 v[14:17], v83
	v_cvt_pk_f16_f32 v5, v4, v5
	v_cvt_pk_f16_f32 v4, v2, v3
	v_cvt_pk_f16_f32 v3, v12, v13
	v_cvt_pk_f16_f32 v2, v10, v11
	ds_read_b128 v[10:13], v83 offset:64
	ds_read_b128 v[22:25], v83 offset:4352
	ds_read_b128 v[26:29], v83 offset:4416
	ds_read_b128 v[30:33], v83 offset:8704
	ds_read_b128 v[50:53], v83 offset:8768
	ds_read_b128 v[54:57], v83 offset:13056
	ds_read_b128 v[58:61], v83 offset:13120
	ds_read_b128 v[62:65], v83 offset:17408
	ds_read_b128 v[72:75], v83 offset:17472
	ds_read_b128 v[76:79], v83 offset:21760
	ds_read_b128 v[92:95], v83 offset:21824
	ds_read_b128 v[96:99], v83 offset:26112
	ds_read_b128 v[100:103], v83 offset:26176
	ds_read_b128 v[104:107], v83 offset:30464
	ds_read_b128 v[110:113], v83 offset:30528
	v_add_u32_e32 v91, 0xfffffa1c, v67
	v_cmp_gt_i32_e64 s[4:5], s3, v91
	s_mov_b64 s[36:37], s[4:5]
	s_waitcnt lgkmcnt(14)
	v_mfma_f32_16x16x32_f16 v[14:17], v[14:17], v[2:5], 0
	v_cvt_pk_f16_f32 v109, v8, v9
	v_cvt_pk_f16_f32 v108, v6, v7
	v_cvt_pk_f16_f32 v49, v48, v49
	s_waitcnt lgkmcnt(13)
	v_mfma_f32_16x16x32_f16 v[22:25], v[22:25], v[2:5], 0
	v_cvt_pk_f16_f32 v48, v46, v47
	v_cvt_pk_f16_f32 v47, v44, v45
	v_cvt_pk_f16_f32 v46, v42, v43
	s_waitcnt lgkmcnt(11)
	v_mfma_f32_16x16x32_f16 v[30:33], v[30:33], v[2:5], 0
	s_waitcnt lgkmcnt(9)
	v_mfma_f32_16x16x32_f16 v[54:57], v[54:57], v[2:5], 0
	s_waitcnt lgkmcnt(7)
	v_mfma_f32_16x16x32_f16 v[62:65], v[62:65], v[2:5], 0
	s_waitcnt lgkmcnt(5)
	v_mfma_f32_16x16x32_f16 v[76:79], v[76:79], v[2:5], 0
	s_waitcnt lgkmcnt(3)
	v_mfma_f32_16x16x32_f16 v[96:99], v[96:99], v[2:5], 0
	s_waitcnt lgkmcnt(1)
	v_mfma_f32_16x16x32_f16 v[114:117], v[104:107], v[2:5], 0
	v_cndmask_b32_e64 v2, v91, v67, s[4:5]
	v_lshl_or_b32 v2, v2, 4, v1
	v_ashrrev_i32_e32 v3, 31, v2
	v_cvt_pk_f16_f32 v107, v20, v21
	v_cvt_pk_f16_f32 v106, v18, v19
	v_lshlrev_b64 v[2:3], 9, v[2:3]
	v_cmp_lt_i32_e64 s[4:5], v85, v86
	v_mfma_f32_16x16x32_f16 v[122:125], v[26:29], v[106:109], v[22:25]
	s_nop 2
	v_lshl_add_u64 v[22:23], v[68:69], 0, v[2:3]
	v_mfma_f32_16x16x32_f16 v[118:121], v[10:13], v[106:109], v[14:17]
	s_cmp_eq_u64 s[36:37], 0
	s_cbranch_scc1 .Lg1_nopfA
	global_load_dwordx4 v[10:13], v[22:23], off
	global_load_dwordx4 v[2:5], v[22:23], off offset:64
	global_load_dwordx4 v[18:21], v[22:23], off offset:128
	global_load_dwordx4 v[6:9], v[22:23], off offset:192
	global_load_dwordx4 v[26:29], v[22:23], off offset:256
	global_load_dwordx4 v[14:17], v[22:23], off offset:320
.Lg1_nopfA:
	v_mfma_f32_16x16x32_f16 v[50:53], v[50:53], v[106:109], v[30:33]
	s_nop 2
	s_cmp_eq_u64 s[36:37], 0
	s_cbranch_scc1 .Lg1_nopfB
	global_load_dwordx4 v[30:33], v[22:23], off offset:384
	s_nop 0
	global_load_dwordx4 v[22:25], v[22:23], off offset:448
.Lg1_nopfB:
	v_mfma_f32_16x16x32_f16 v[54:57], v[58:61], v[106:109], v[54:57]
	v_mfma_f32_16x16x32_f16 v[58:61], v[72:75], v[106:109], v[62:65]
	ds_read_b128 v[72:75], v83 offset:128
	v_mfma_f32_16x16x32_f16 v[62:65], v[92:95], v[106:109], v[76:79]
	ds_read_b128 v[92:95], v83 offset:4480
	v_mfma_f32_16x16x32_f16 v[76:79], v[100:103], v[106:109], v[96:99]
	ds_read_b128 v[42:45], v83 offset:8832
	ds_read_b128 v[100:103], v83 offset:192
	s_waitcnt lgkmcnt(4)
	v_mfma_f32_16x16x32_f16 v[96:99], v[110:113], v[106:109], v[114:117]
	ds_read_b128 v[104:107], v83 offset:13184
	ds_read_b128 v[108:111], v83 offset:17536
	s_nop 0
	ds_read_b128 v[112:115], v83 offset:4544
	s_waitcnt lgkmcnt(5)
	v_mfma_f32_16x16x32_f16 v[92:95], v[92:95], v[46:49], v[122:125]
	s_nop 2
	ds_read_b128 v[124:127], v83 offset:8896
	v_mfma_f32_16x16x32_f16 v[72:75], v[72:75], v[46:49], v[118:121]
	v_cvt_pk_f16_f32 v123, v40, v41
	v_cvt_pk_f16_f32 v122, v38, v39
	s_nop 0
	ds_read_b128 v[116:119], v83 offset:21888
	s_waitcnt lgkmcnt(6)
	v_mfma_f32_16x16x32_f16 v[42:45], v[42:45], v[46:49], v[50:53]
	v_cvt_pk_f16_f32 v121, v36, v37
	v_cvt_pk_f16_f32 v120, v34, v35
	v_cndmask_b32_e64 v34, v84, v85, s[4:5]
	ds_read_b128 v[50:53], v83 offset:13248
	s_waitcnt lgkmcnt(5)
	v_mfma_f32_16x16x32_f16 v[54:57], v[104:107], v[46:49], v[54:57]
	ds_read_b128 v[104:107], v83 offset:17600
	ds_read_b128 v[128:131], v83 offset:21952
	v_lshlrev_b32_e32 v144, 2, v34
	v_cmp_lt_i32_e64 s[4:5], v87, v86
	s_waitcnt lgkmcnt(6)
	v_mfma_f32_16x16x32_f16 v[58:61], v[108:111], v[46:49], v[58:61]
	ds_read_b128 v[108:111], v83 offset:26240
	ds_read_b128 v[132:135], v83 offset:26304
	ds_read_b128 v[136:139], v83 offset:30592
	ds_read_b128 v[140:143], v83 offset:30656
	v_cndmask_b32_e64 v145, v84, v87, s[4:5]
	v_mfma_f32_16x16x32_f16 v[38:41], v[100:103], v[120:123], v[72:75]
	s_nop 2
	ds_read_b128 v[72:75], v66 offset:52736
	ds_read_b128 v[100:103], v66 offset:52800
	s_waitcnt lgkmcnt(10)
	v_mfma_f32_16x16x32_f16 v[34:37], v[124:127], v[120:123], v[42:45]
	ds_read_b128 v[124:127], v66 offset:52864
	s_waitcnt lgkmcnt(6)
	v_mfma_f32_16x16x32_f16 v[76:79], v[108:111], v[46:49], v[76:79]
	ds_read_b128 v[108:111], v66 offset:52928
	v_mov_b32_e32 v42, v38
	s_nop 2
	v_mov_b32_e32 v43, v34
	v_mfma_f32_16x16x32_f16 v[116:119], v[116:119], v[46:49], v[62:65]
	s_waitcnt lgkmcnt(3)
	v_mov_b32_e32 v44, v72
	s_waitcnt lgkmcnt(1)
	v_mov_b32_e32 v45, v124
	v_pk_fma_f32 v[42:43], v[42:43], v[44:45], 0 op_sel_hi:[1,1,0]
	v_mfma_f32_16x16x32_f16 v[62:65], v[112:115], v[120:123], v[92:95]
	v_mov_b32_e32 v44, v39
	v_mov_b32_e32 v45, v35
	v_mov_b32_e32 v124, v73
	v_mfma_f32_16x16x32_f16 v[54:57], v[50:53], v[120:123], v[54:57]
	v_mov_b32_e32 v50, v74
	v_mov_b32_e32 v51, v126
	v_mov_b32_e32 v52, v41
	v_mfma_f32_16x16x32_f16 v[96:99], v[136:139], v[46:49], v[96:99]
	v_fma_f32 v46, v44, v124, v42
	v_fma_f32 v47, v45, v125, v43
	v_mov_b32_e32 v48, v40
	v_mov_b32_e32 v49, v36
	v_pk_fma_f32 v[50:51], v[48:49], v[50:51], v[46:47]
	v_mov_b32_e32 v53, v37
	v_mov_b32_e32 v126, v75
	v_pk_fma_f32 v[72:73], v[52:53], v[126:127], v[50:51]
	v_mov_b32_e32 v74, v62
	v_mfma_f32_16x16x32_f16 v[50:53], v[132:135], v[120:123], v[76:79]
	v_mov_b32_e32 v75, v54
	s_nop 1
	v_mov_b32_e32 v76, v100
	s_waitcnt lgkmcnt(0)
	v_mov_b32_e32 v77, v108
	v_pk_fma_f32 v[72:73], v[74:75], v[76:77], v[72:73]
	v_mov_b32_e32 v74, v63
	v_mov_b32_e32 v75, v55
	v_mov_b32_e32 v108, v101
	v_pk_fma_f32 v[72:73], v[74:75], v[108:109], v[72:73]
	v_mov_b32_e32 v74, v64
	v_mov_b32_e32 v75, v56
	v_mov_b32_e32 v76, v102
	v_mov_b32_e32 v77, v110
	v_pk_fma_f32 v[72:73], v[74:75], v[76:77], v[72:73]
	v_mov_b32_e32 v74, v65
	v_mov_b32_e32 v75, v57
	v_mov_b32_e32 v110, v103
	v_pk_fma_f32 v[100:101], v[74:75], v[110:111], v[72:73]
	ds_read_b128 v[72:75], v66 offset:52992
	ds_read_b128 v[76:79], v66 offset:53056
	ds_read_b128 v[92:95], v66 offset:53120
	v_mfma_f32_16x16x32_f16 v[42:45], v[104:107], v[120:123], v[58:61]
	v_mov_b32_e32 v105, v50
	s_waitcnt lgkmcnt(2)
	v_mov_b32_e32 v106, v72
	ds_bpermute_b32 v102, v144, v100
	v_mfma_f32_16x16x32_f16 v[58:61], v[140:143], v[120:123], v[96:99]
	s_waitcnt lgkmcnt(1)
	v_mov_b32_e32 v107, v92
	s_nop 0
	v_mov_b32_e32 v104, v42
	v_pk_fma_f32 v[104:105], v[104:105], v[106:107], 0 op_sel_hi:[1,1,0]
	ds_read_b128 v[96:99], v66 offset:53184
	v_mfma_f32_16x16x32_f16 v[46:49], v[128:131], v[120:123], v[116:119]
	v_mov_b32_e32 v106, v43
	v_mov_b32_e32 v107, v51
	v_mov_b32_e32 v92, v73
	v_pk_fma_f32 v[72:73], v[106:107], v[92:93], v[104:105]
	v_mov_b32_e32 v92, v44
	v_mov_b32_e32 v93, v52
	v_mov_b32_e32 v104, v74
	v_mov_b32_e32 v105, v94
	v_pk_fma_f32 v[72:73], v[92:93], v[104:105], v[72:73]
	v_mov_b32_e32 v92, v45
	v_mov_b32_e32 v93, v53
	v_mov_b32_e32 v94, v75
	v_pk_fma_f32 v[72:73], v[92:93], v[94:95], v[72:73]
	v_mov_b32_e32 v74, v46
	v_mov_b32_e32 v75, v58
	v_mov_b32_e32 v92, v76
	s_waitcnt lgkmcnt(0)
	v_mov_b32_e32 v93, v96
	v_pk_fma_f32 v[72:73], v[74:75], v[92:93], v[72:73]
	v_mov_b32_e32 v74, v47
	v_mov_b32_e32 v75, v59
	v_mov_b32_e32 v96, v77
	v_pk_fma_f32 v[72:73], v[74:75], v[96:97], v[72:73]
	v_mov_b32_e32 v74, v48
	v_mov_b32_e32 v75, v60
	v_mov_b32_e32 v76, v78
	v_mov_b32_e32 v77, v98
	v_pk_fma_f32 v[72:73], v[74:75], v[76:77], v[72:73]
	v_mov_b32_e32 v74, v49
	v_mov_b32_e32 v75, v61
	v_mov_b32_e32 v98, v79
	v_pk_fma_f32 v[76:77], v[74:75], v[98:99], v[72:73]
	ds_bpermute_b32 v103, v144, v101
	ds_bpermute_b32 v78, v144, v76
	ds_bpermute_b32 v79, v144, v77
	v_lshlrev_b32_e32 v92, 2, v145
	s_waitcnt lgkmcnt(2)
	v_pk_add_f32 v[72:73], v[100:101], v[102:103]
	ds_bpermute_b32 v74, v92, v72
	s_waitcnt lgkmcnt(1)
	v_pk_add_f32 v[76:77], v[76:77], v[78:79]
	ds_bpermute_b32 v75, v92, v73
	ds_bpermute_b32 v78, v92, v76
	ds_bpermute_b32 v79, v92, v77
	s_and_saveexec_b64 s[4:5], vcc
	s_cbranch_execz .LBB1_18
	v_add_u32_e32 v92, v81, v82
	v_ashrrev_i32_e32 v93, 31, v92
	v_lshl_add_u64 v[92:93], v[92:93], 4, s[8:9]
	s_waitcnt lgkmcnt(2)
	v_pk_add_f32 v[72:73], v[72:73], v[74:75]
	s_waitcnt lgkmcnt(0)
	v_pk_add_f32 v[74:75], v[76:77], v[78:79]
	global_store_dwordx4 v[92:93], v[72:75], off
	s_branch .LBB1_18

.LBB2_19:
	ds_read_b128 v[14:17], v83
	v_cvt_pk_f16_f32 v5, v4, v5
	v_cvt_pk_f16_f32 v4, v2, v3
	v_cvt_pk_f16_f32 v3, v12, v13
	v_cvt_pk_f16_f32 v2, v10, v11
	ds_read_b128 v[10:13], v83 offset:64
	ds_read_b128 v[22:25], v83 offset:4352
	ds_read_b128 v[42:45], v83 offset:4416
	ds_read_b128 v[46:49], v83 offset:8704
	ds_read_b128 v[50:53], v83 offset:8768
	ds_read_b128 v[54:57], v83 offset:13056
	ds_read_b128 v[58:61], v83 offset:13120
	ds_read_b128 v[62:65], v83 offset:17408
	ds_read_b128 v[72:75], v83 offset:17472
	ds_read_b128 v[76:79], v83 offset:21760
	ds_read_b128 v[92:95], v83 offset:21824
	ds_read_b128 v[96:99], v83 offset:26112
	ds_read_b128 v[100:103], v83 offset:26176
	ds_read_b128 v[104:107], v83 offset:30464
	ds_read_b128 v[110:113], v83 offset:30528
	v_mov_b32_e32 v91, v1
	v_add_u32_e32 v1, 0x5e4, v91
	v_cmp_gt_i32_e64 s[4:5], s14, v91
	s_mov_b64 s[36:37], s[4:5]
	s_waitcnt lgkmcnt(14)
	v_mfma_f32_16x16x32_f16 v[14:17], v[14:17], v[2:5], 0
	v_cvt_pk_f16_f32 v109, v8, v9
	v_cvt_pk_f16_f32 v108, v6, v7
	v_cvt_pk_f16_f32 v127, v40, v41
	s_waitcnt lgkmcnt(13)
	v_mfma_f32_16x16x32_f16 v[22:25], v[22:25], v[2:5], 0
	v_cvt_pk_f16_f32 v126, v38, v39
	v_cvt_pk_f16_f32 v125, v36, v37
	v_cvt_pk_f16_f32 v124, v34, v35
	s_waitcnt lgkmcnt(11)
	v_mfma_f32_16x16x32_f16 v[46:49], v[46:49], v[2:5], 0
	s_waitcnt lgkmcnt(9)
	v_mfma_f32_16x16x32_f16 v[54:57], v[54:57], v[2:5], 0
	s_waitcnt lgkmcnt(7)
	v_mfma_f32_16x16x32_f16 v[62:65], v[62:65], v[2:5], 0
	s_waitcnt lgkmcnt(5)
	v_mfma_f32_16x16x32_f16 v[76:79], v[76:79], v[2:5], 0
	s_waitcnt lgkmcnt(3)
	v_mfma_f32_16x16x32_f16 v[96:99], v[96:99], v[2:5], 0
	s_waitcnt lgkmcnt(1)
	v_mfma_f32_16x16x32_f16 v[114:117], v[104:107], v[2:5], 0
	v_cndmask_b32_e64 v2, v91, v1, s[4:5]
	v_lshl_or_b32 v2, v2, 4, v80
	v_ashrrev_i32_e32 v3, 31, v2
	v_lshlrev_b64 v[2:3], 9, v[2:3]
	v_cvt_pk_f16_f32 v107, v20, v21
	v_cvt_pk_f16_f32 v106, v18, v19
	v_lshl_add_u64 v[122:123], v[68:69], 0, v[2:3]
	v_cmp_lt_i32_e64 s[4:5], v85, v86
	v_mfma_f32_16x16x32_f16 v[118:121], v[10:13], v[106:109], v[14:17]
	s_cmp_eq_u64 s[36:37], 0
	s_cbranch_scc1 .Lg2_nopfA
	global_load_dwordx4 v[10:13], v[122:123], off
	global_load_dwordx4 v[2:5], v[122:123], off offset:64
	global_load_dwordx4 v[18:21], v[122:123], off offset:128
	global_load_dwordx4 v[6:9], v[122:123], off offset:192
.Lg2_nopfA:
	v_cndmask_b32_e64 v34, v84, v85, s[4:5]
	v_lshlrev_b32_e32 v142, 2, v34
	v_mfma_f32_16x16x32_f16 v[42:45], v[42:45], v[106:109], v[22:25]
	s_nop 2
	s_cmp_eq_u64 s[36:37], 0
	s_cbranch_scc1 .Lg2_nopfB
	global_load_dwordx4 v[22:25], v[122:123], off offset:256
	global_load_dwordx4 v[14:17], v[122:123], off offset:320
.Lg2_nopfB:
	v_cmp_lt_i32_e64 s[4:5], v87, v86
	v_mfma_f32_16x16x32_f16 v[46:49], v[50:53], v[106:109], v[46:49]
	s_nop 0
	v_cndmask_b32_e64 v143, v84, v87, s[4:5]
	v_cmp_lt_i32_e64 s[4:5], s3, v91
	v_mfma_f32_16x16x32_f16 v[50:53], v[58:61], v[106:109], v[54:57]
	v_mfma_f32_16x16x32_f16 v[54:57], v[72:75], v[106:109], v[62:65]
	ds_read_b128 v[72:75], v83 offset:128
	v_mfma_f32_16x16x32_f16 v[58:61], v[92:95], v[106:109], v[76:79]
	s_nop 0
	v_cvt_pk_f16_f32 v65, v28, v29
	v_cvt_pk_f16_f32 v64, v26, v27
	v_cvt_pk_f16_f32 v63, v32, v33
	v_mfma_f32_16x16x32_f16 v[76:79], v[100:103], v[106:109], v[96:99]
	ds_read_b128 v[92:95], v83 offset:4480
	v_cvt_pk_f16_f32 v62, v30, v31
	s_waitcnt lgkmcnt(2)
	v_mfma_f32_16x16x32_f16 v[96:99], v[110:113], v[106:109], v[114:117]
	ds_read_b128 v[100:103], v83 offset:8832
	ds_read_b128 v[104:107], v83 offset:192
	s_cmp_eq_u64 s[36:37], 0
	s_cbranch_scc1 .Lg2_nopfC
	global_load_dwordx4 v[30:33], v[122:123], off offset:384
	global_load_dwordx4 v[26:29], v[122:123], off offset:448
.Lg2_nopfC:
	ds_read_b128 v[108:111], v83 offset:13184
	ds_read_b128 v[112:115], v83 offset:4544
	s_waitcnt lgkmcnt(5)
	v_mfma_f32_16x16x32_f16 v[72:75], v[72:75], v[62:65], v[118:121]
	s_waitcnt lgkmcnt(4)
	v_mfma_f32_16x16x32_f16 v[42:45], v[92:95], v[62:65], v[42:45]
	ds_read_b128 v[92:95], v83 offset:17536
	ds_read_b128 v[116:119], v83 offset:21888
	ds_read_b128 v[120:123], v83 offset:8896
	ds_read_b128 v[128:131], v83 offset:13248
	s_waitcnt lgkmcnt(7)
	v_mfma_f32_16x16x32_f16 v[46:49], v[100:103], v[62:65], v[46:49]
	ds_read_b128 v[100:103], v83 offset:26240
	s_waitcnt lgkmcnt(6)
	v_mfma_f32_16x16x32_f16 v[50:53], v[108:111], v[62:65], v[50:53]
	ds_read_b128 v[108:111], v83 offset:17600
	ds_read_b128 v[132:135], v83 offset:21952
	ds_read_b128 v[136:139], v83 offset:26304
	s_waitcnt lgkmcnt(7)
	v_mfma_f32_16x16x32_f16 v[92:95], v[92:95], v[62:65], v[54:57]
	s_waitcnt lgkmcnt(6)
	v_mfma_f32_16x16x32_f16 v[58:61], v[116:119], v[62:65], v[58:61]
	s_nop 0
	ds_read_b128 v[54:57], v83 offset:30592
	ds_read_b128 v[116:119], v83 offset:30656
	s_waitcnt lgkmcnt(5)
	v_mfma_f32_16x16x32_f16 v[76:79], v[100:103], v[62:65], v[76:79]
	v_mfma_f32_16x16x32_f16 v[38:41], v[104:107], v[124:127], v[72:75]
	s_nop 2
	ds_read_b128 v[72:75], v66 offset:52736
	ds_read_b128 v[100:103], v66 offset:52800
	ds_read_b128 v[104:107], v66 offset:52864
	s_nop 1
	v_mov_b32_e32 v140, v38
	v_mfma_f32_16x16x32_f16 v[34:37], v[120:123], v[124:127], v[46:49]
	ds_read_b128 v[120:123], v66 offset:52928
	s_waitcnt lgkmcnt(3)
	s_nop 0
	v_mov_b32_e32 v46, v72
	v_mfma_f32_16x16x32_f16 v[96:99], v[54:57], v[62:65], v[96:99]
	s_nop 2
	v_mov_b32_e32 v141, v34
	s_waitcnt lgkmcnt(1)
	v_mov_b32_e32 v47, v104
	v_pk_fma_f32 v[46:47], v[140:141], v[46:47], 0 op_sel_hi:[1,1,0]
	v_mfma_f32_16x16x32_f16 v[62:65], v[112:115], v[124:127], v[42:45]
	v_mov_b32_e32 v48, v39
	v_mov_b32_e32 v49, v35
	v_mov_b32_e32 v104, v73
	v_mfma_f32_16x16x32_f16 v[54:57], v[128:131], v[124:127], v[50:53]
	v_fma_f32 v42, v48, v104, v46
	v_fma_f32 v43, v49, v105, v47
	v_mov_b32_e32 v44, v40
	v_mov_b32_e32 v45, v36
	v_mov_b32_e32 v50, v74
	v_mov_b32_e32 v51, v106
	v_pk_fma_f32 v[42:43], v[44:45], v[50:51], v[42:43]
	v_mov_b32_e32 v44, v41
	v_mov_b32_e32 v45, v37
	v_mov_b32_e32 v106, v75
	v_pk_fma_f32 v[72:73], v[44:45], v[106:107], v[42:43]
	v_mfma_f32_16x16x32_f16 v[42:45], v[136:139], v[124:127], v[76:79]
	v_mov_b32_e32 v74, v62
	v_mov_b32_e32 v75, v54
	s_nop 0
	v_mov_b32_e32 v76, v100
	s_waitcnt lgkmcnt(0)
	v_mov_b32_e32 v77, v120
	v_pk_fma_f32 v[72:73], v[74:75], v[76:77], v[72:73]
	v_mov_b32_e32 v74, v63
	v_mov_b32_e32 v75, v55
	v_mov_b32_e32 v120, v101
	v_pk_fma_f32 v[72:73], v[74:75], v[120:121], v[72:73]
	v_mov_b32_e32 v74, v64
	v_mov_b32_e32 v75, v56
	v_mov_b32_e32 v76, v102
	v_mov_b32_e32 v77, v122
	v_pk_fma_f32 v[72:73], v[74:75], v[76:77], v[72:73]
	v_mov_b32_e32 v74, v65
	v_mov_b32_e32 v75, v57
	v_mov_b32_e32 v122, v103
	v_mfma_f32_16x16x32_f16 v[46:49], v[108:111], v[124:127], v[92:95]
	v_fma_f32 v100, v74, v122, v72
	v_fma_f32 v101, v75, v123, v73
	ds_read_b128 v[72:75], v66 offset:52992
	ds_read_b128 v[76:79], v66 offset:53056
	ds_read_b128 v[92:95], v66 offset:53120
	v_mov_b32_e32 v105, v42
	v_mfma_f32_16x16x32_f16 v[50:53], v[132:135], v[124:127], v[58:61]
	s_nop 0
	v_mov_b32_e32 v104, v46
	s_waitcnt lgkmcnt(2)
	v_mov_b32_e32 v106, v72
	s_waitcnt lgkmcnt(0)
	v_mov_b32_e32 v107, v92
	v_mfma_f32_16x16x32_f16 v[58:61], v[116:119], v[124:127], v[96:99]
	v_fma_f32 v104, v104, v106, 0
	v_fma_f32 v105, v105, v107, 0
	v_mov_b32_e32 v106, v47
	v_mov_b32_e32 v107, v43
	ds_read_b128 v[96:99], v66 offset:53184
	v_mov_b32_e32 v92, v73
	v_pk_fma_f32 v[72:73], v[106:107], v[92:93], v[104:105]
	v_mov_b32_e32 v92, v48
	v_mov_b32_e32 v93, v44
	v_mov_b32_e32 v104, v74
	v_mov_b32_e32 v105, v94
	v_pk_fma_f32 v[72:73], v[92:93], v[104:105], v[72:73]
	v_mov_b32_e32 v92, v49
	v_mov_b32_e32 v93, v45
	v_mov_b32_e32 v94, v75
	v_pk_fma_f32 v[72:73], v[92:93], v[94:95], v[72:73]
	v_mov_b32_e32 v74, v50
	v_mov_b32_e32 v75, v58
	v_mov_b32_e32 v92, v76
	s_waitcnt lgkmcnt(0)
	v_mov_b32_e32 v93, v96
	v_pk_fma_f32 v[72:73], v[74:75], v[92:93], v[72:73]
	v_mov_b32_e32 v74, v51
	v_mov_b32_e32 v75, v59
	v_mov_b32_e32 v96, v77
	v_pk_fma_f32 v[72:73], v[74:75], v[96:97], v[72:73]
	v_mov_b32_e32 v74, v52
	v_mov_b32_e32 v75, v60
	v_mov_b32_e32 v76, v78
	v_mov_b32_e32 v77, v98
	v_pk_fma_f32 v[72:73], v[74:75], v[76:77], v[72:73]
	v_mov_b32_e32 v74, v53
	v_mov_b32_e32 v75, v61
	v_mov_b32_e32 v98, v79
	v_pk_fma_f32 v[76:77], v[74:75], v[98:99], v[72:73]
	ds_bpermute_b32 v102, v142, v100
	ds_bpermute_b32 v103, v142, v101
	ds_bpermute_b32 v78, v142, v76
	ds_bpermute_b32 v79, v142, v77
	v_lshlrev_b32_e32 v92, 2, v143
	s_waitcnt lgkmcnt(2)
	v_pk_add_f32 v[72:73], v[100:101], v[102:103]
	ds_bpermute_b32 v74, v92, v72
	s_waitcnt lgkmcnt(1)
	v_pk_add_f32 v[76:77], v[76:77], v[78:79]
	ds_bpermute_b32 v75, v92, v73
	ds_bpermute_b32 v78, v92, v76
	ds_bpermute_b32 v79, v92, v77
	s_and_saveexec_b64 s[12:13], vcc
	s_cbranch_execz .LBB2_18
	v_add_u32_e32 v92, v67, v82
	v_ashrrev_i32_e32 v93, 31, v92
	v_lshl_add_u64 v[92:93], v[92:93], 4, s[8:9]
	s_waitcnt lgkmcnt(2)
	v_pk_add_f32 v[72:73], v[72:73], v[74:75]
	s_waitcnt lgkmcnt(0)
	v_pk_add_f32 v[74:75], v[76:77], v[78:79]
	global_store_dwordx4 v[92:93], v[72:75], off
	s_branch .LBB2_18
